# MoBA-C exit: GLA-B-done flag re-read by thread 0 once per item and taken early at the loop exit when already set (original wait kept as fallback)
# speedup vs baseline: 1.0052x; 1.0034x over previous
.LBB0_1053:
	s_nop 0
	s_nop 0
	s_nop 0
	s_nop 0
	s_nop 0
	v_and_b32_e32 v3, 64, v68
	v_xor_b32_e32 v2, 32, v68
	v_add_u32_e32 v3, 64, v3
	v_cmp_lt_i32_e32 vcc, v2, v3
	s_mov_b64 s[20:21], -1
	s_mov_b64 s[22:23], -1
	v_cndmask_b32_e32 v2, v68, v2, vcc
	v_lshlrev_b32_e32 v2, 2, v2
	ds_bpermute_b32 v6, v2, v71
	ds_bpermute_b32 v5, v2, v50
	ds_bpermute_b32 v3, v2, v57
	ds_bpermute_b32 v7, v2, v69
	ds_bpermute_b32 v4, v2, v59
	ds_bpermute_b32 v2, v2, v70
	s_waitcnt lgkmcnt(5)
	v_cmp_nlt_f32_e32 vcc, v71, v6
	s_and_saveexec_b64 s[18:19], vcc
	s_cbranch_execz .LBB0_1057
	v_cmp_eq_f32_e32 vcc, v71, v6
	s_mov_b64 s[22:23], 0
	s_and_saveexec_b64 s[24:25], vcc
	s_cbranch_execz .LBB0_1056
	s_waitcnt lgkmcnt(2)
	v_cmp_lt_i32_e32 vcc, v7, v69
	s_and_b64 s[22:23], vcc, exec

.LBB0_1364:
	v_mov_b32_e32 v247, 0
	s_lshl_b32 s100, s89, 6
	s_add_u32 s100, s46, s100
	s_addc_u32 s101, s47, 0
	v_and_b32_e32 v156, 31, v0
	s_cmp_ge_i32 s6, s8
	v_lshrrev_b32_e32 v157, 5, v248
	s_cbranch_scc1 .LBB0_1393
	s_movk_i32 s0, 0xff
	s_mov_b32 s10, 0

.Lmc_bottom:
	s_and_saveexec_b64 s[98:99], s[40:41]
	v_mov_b32_e32 v246, 0xb000
	global_load_dword v247, v246, s[100:101] offset:2304 sc1
	s_mov_b64 exec, s[98:99]
	v_mov_b64_e32 v[82:83], v[142:143]
	v_mov_b64_e32 v[86:87], v[138:139]
	v_mov_b64_e32 v[90:91], v[134:135]
	v_mov_b64_e32 v[94:95], v[130:131]
	v_mov_b64_e32 v[98:99], v[126:127]
	v_mov_b64_e32 v[102:103], v[122:123]
	v_mov_b64_e32 v[106:107], v[118:119]
	v_mov_b64_e32 v[110:111], v[114:115]
	s_andn2_b64 vcc, exec, s[18:19]
	v_mov_b64_e32 v[84:85], v[144:145]
	v_mov_b64_e32 v[88:89], v[140:141]
	v_mov_b64_e32 v[92:93], v[136:137]
	v_mov_b64_e32 v[96:97], v[132:133]
	v_mov_b64_e32 v[100:101], v[128:129]
	v_mov_b64_e32 v[104:105], v[124:125]
	v_mov_b64_e32 v[108:109], v[120:121]
	v_mov_b64_e32 v[112:113], v[116:117]
	s_mov_b64 s[14:15], s[20:21]
	s_mov_b64 s[24:25], s[22:23]
	v_mov_b32_e32 v155, v151
	v_mov_b32_e32 v148, v153
	s_cbranch_vccz .LBB0_1393

.LBB0_1393:
	s_waitcnt lgkmcnt(0)
	s_barrier
	s_and_b64 vcc, exec, s[42:43]
	s_cbranch_vccnz .LBB0_1410
	s_and_saveexec_b64 s[0:1], s[40:41]
	s_cbranch_execz .LBB0_1409
	s_waitcnt vmcnt(0)
	v_cmp_ne_u32_e32 vcc, 0, v247
	s_cbranch_vccnz .LBB0_1408
	s_lshl_b32 s4, s89, 6
	s_add_u32 s4, s46, s4
	s_addc_u32 s5, s47, 0
	v_mov_b32_e32 v2, 0xb000
	global_load_dword v2, v2, s[4:5] offset:2304 sc1
	s_add_u32 s4, s4, 0xb900
	s_addc_u32 s5, s5, 0
	s_waitcnt vmcnt(0)
	v_cmp_ne_u32_e32 vcc, 0, v2
	s_cbranch_vccnz .LBB0_1408
	s_mov_b32 s12, 1
	v_mov_b32_e32 v2, 0
	s_branch .LBB0_1398
